# in3: dma1 + IN GEMM main loop: LDS-DMA stage loads addressed by scalar base + 32-bit lane offset (16 v_lshl_add_u64 per two K tiles removed)
# baseline (speedup 1.0000x reference)
; #define PG8_STAGE(bufoff, gbase, voff) do { _Pragma("unroll") for (int _i = 0; _i < 2; ++_i) \
;         __builtin_amdgcn_global_load_lds((const unsigned*)((const char*)(gbase) + (voff)[_i]), (LAS unsigned*)(lds + (bufoff) + ldsw + _i * 8192), 16, 0, 0); } while (0)
; #define PG8_STAGE_A(bufoff, gbase, h, nx) do { if constexpr (GATHER) { unsigned _v[2]; _v[0] = (nx) ? voffAn[h][0] : voffA[h][0]; _v[1] = (nx) ? voffAn[h][1] : voffA[h][1]; PG8_STAGE(bufoff, gbase, _v); } \
;         else PG8_STAGE(bufoff, (gbase) + (h) * hstepA, voffA[0]); } while (0)
; #define PG8_LDA(dst, b, h) do { _Pragma("unroll") for (int m = 0; m < 4; ++m) _Pragma("unroll") for (int k = 0; k < 2; ++k) dst[m][k] = *(const LAS bf16x8*)(lds + PG8_SA(b, h) + aoff + m * 2048 + k * 1024); } while (0)
; #define PG8_LDB(dst, b, h) do { _Pragma("unroll") for (int n = 0; n < 2; ++n) _Pragma("unroll") for (int k = 0; k < 2; ++k) dst[n][k] = *(const LAS bf16x8*)(lds + PG8_SB(b, h) + boff + n * 2048 + k * 1024); } while (0)
; #define PG8_WAIT_V(n) asm volatile("s_waitcnt vmcnt(" #n ")" ::: "memory")
; #define PG8_WAIT_L(n) asm volatile("s_waitcnt lgkmcnt(" #n ")" ::: "memory")
; #define PG8_BAR __builtin_amdgcn_s_barrier()
; #define PG8_SCHED __builtin_amdgcn_sched_barrier(0)
; template <class Epi, class Sched, bool GATHER, bool ALIGN_EPI>
; __device__ __forceinline__ void gemm_phase(LAS unsigned char* lds, const int wave_, const int K, const int lda, const int ldb, const Sched& S, const Epi& E) {
;     ...
;             const bool last = (t == nt - 2);
;             const char* a1 = cA + (size_t)(t + 1) * kstep;
;             const char* a2 = last ? nA : cA + (size_t)(t + 2) * kstep; const char* b2 = last ? nB : cB + (size_t)(t + 2) * kstep;
;             const char* a3 = a2 + kstep; const char* b3 = b2 + kstep;
;             if (last && has_next) S.a_ready(nxt);
;             PG8_LDB(B0, 0, 0); PG8_LDB(B1, 0, 1); PG8_SCHED; PG8_LDA(At, 0, 0); PG8_STAGE_A(PG8_SA(1, 1), a1, 1, false);
;             PG8_WAIT_V(8); PG8_WAIT_L(0); PG8_BAR; PG8_MMA(0, 0, At, B0); PG8_MMA(0, 1, At, B1); PG8_BAR; PG8_SCHED;
;             PG8_LDA(At, 0, 1); PG8_STAGE(PG8_SB(0, 0), b2, voffB); PG8_STAGE(PG8_SB(0, 1), b2 + hstepB, voffB); PG8_STAGE_A(PG8_SA(0, 0), a2, 0, last);
;             PG8_WAIT_V(8); PG8_WAIT_L(0); PG8_BAR; PG8_MMA(1, 0, At, B0); PG8_MMA(1, 1, At, B1); PG8_BAR; PG8_SCHED;
.LBB0_720:
	s_add_u32 s2, s4, 0xfffc0080
	s_addc_u32 s3, s5, -1
	s_cmp_eq_u32 s31, 12
	s_cselect_b32 s21, s15, s3
	s_cselect_b32 s20, s14, s2
	s_cselect_b32 s19, s17, s13
	s_cselect_b32 s18, s16, s11
	s_add_i32 s2, 0, 0x10000
	s_add_i32 s8, 0, 0x14000
	v_add_u32_e32 v140, s2, v201
	v_add_u32_e32 v160, s8, v201
	ds_read_b128 v[128:131], v140
	ds_read_b128 v[132:135], v140 offset:1024
	ds_read_b128 v[136:139], v140 offset:2048
	ds_read_b128 v[140:143], v140 offset:3072
	ds_read_b128 v[144:147], v160
	ds_read_b128 v[148:151], v160 offset:1024
	ds_read_b128 v[152:155], v160 offset:2048
	ds_read_b128 v[176:179], v160 offset:3072
	s_add_i32 m0, s22, 0xc000
	ds_read_b128 v[180:183], v215
	ds_read_b128 v[184:187], v215 offset:1024
	ds_read_b128 v[204:207], v215 offset:2048
	ds_read_b128 v[216:219], v215 offset:3072
	ds_read_b128 v[220:223], v215 offset:4096
	ds_read_b128 v[224:227], v215 offset:5120
	ds_read_b128 v[228:231], v215 offset:6144
	ds_read_b128 v[232:235], v215 offset:7168
	global_load_lds_dwordx4 v172, s[4:5]
	s_add_i32 m0, s22, 0xe000
	s_nop 0
	global_load_lds_dwordx4 v174, s[4:5]
	s_waitcnt vmcnt(8)
	s_waitcnt lgkmcnt(0)
	s_barrier
	s_setprio 1
	s_waitcnt lgkmcnt(0)
	v_mfma_f32_16x16x32_bf16 v[124:127], v[128:131], v[180:183], v[124:127]
	v_mfma_f32_16x16x32_bf16 v[120:123], v[136:139], v[180:183], v[120:123]
	v_mfma_f32_16x16x32_bf16 v[108:111], v[128:131], v[204:207], v[108:111]
	v_mfma_f32_16x16x32_bf16 v[104:107], v[136:139], v[204:207], v[104:107]
	v_mfma_f32_16x16x32_bf16 v[92:95], v[128:131], v[220:223], v[92:95]
	v_mfma_f32_16x16x32_bf16 v[88:91], v[136:139], v[220:223], v[88:91]
	v_mfma_f32_16x16x32_bf16 v[76:79], v[128:131], v[228:231], v[76:79]
	v_mfma_f32_16x16x32_bf16 v[72:75], v[136:139], v[228:231], v[72:75]
	v_mfma_f32_16x16x32_bf16 v[124:127], v[132:135], v[184:187], v[124:127]
	v_mfma_f32_16x16x32_bf16 v[120:123], v[140:143], v[184:187], v[120:123]
	v_mfma_f32_16x16x32_bf16 v[108:111], v[132:135], v[216:219], v[108:111]
	v_mfma_f32_16x16x32_bf16 v[104:107], v[140:143], v[216:219], v[104:107]
	v_mfma_f32_16x16x32_bf16 v[92:95], v[132:135], v[224:227], v[92:95]
	v_mfma_f32_16x16x32_bf16 v[88:91], v[140:143], v[224:227], v[88:91]
	v_mfma_f32_16x16x32_bf16 v[76:79], v[132:135], v[232:235], v[76:79]
	v_mfma_f32_16x16x32_bf16 v[72:75], v[140:143], v[232:235], v[72:75]
	s_setprio 0
	s_setprio 1
	v_mfma_f32_16x16x32_bf16 v[116:119], v[144:147], v[180:183], v[116:119]
	v_mfma_f32_16x16x32_bf16 v[112:115], v[152:155], v[180:183], v[112:115]
	v_mfma_f32_16x16x32_bf16 v[100:103], v[144:147], v[204:207], v[100:103]
	v_mfma_f32_16x16x32_bf16 v[96:99], v[152:155], v[204:207], v[96:99]
	v_mfma_f32_16x16x32_bf16 v[84:87], v[144:147], v[220:223], v[84:87]
	v_mfma_f32_16x16x32_bf16 v[80:83], v[152:155], v[220:223], v[80:83]
	v_mfma_f32_16x16x32_bf16 v[68:71], v[144:147], v[228:231], v[68:71]
	v_mfma_f32_16x16x32_bf16 v[64:67], v[152:155], v[228:231], v[64:67]
	v_mfma_f32_16x16x32_bf16 v[116:119], v[148:151], v[184:187], v[116:119]
	v_mfma_f32_16x16x32_bf16 v[112:115], v[176:179], v[184:187], v[112:115]
	v_mfma_f32_16x16x32_bf16 v[100:103], v[148:151], v[216:219], v[100:103]
	v_mfma_f32_16x16x32_bf16 v[96:99], v[176:179], v[216:219], v[96:99]
	v_mfma_f32_16x16x32_bf16 v[84:87], v[148:151], v[224:227], v[84:87]
	v_mfma_f32_16x16x32_bf16 v[80:83], v[176:179], v[224:227], v[80:83]
	v_mfma_f32_16x16x32_bf16 v[68:71], v[148:151], v[232:235], v[68:71]
	v_mfma_f32_16x16x32_bf16 v[64:67], v[176:179], v[232:235], v[64:67]
	s_setprio 0
	s_barrier
	s_add_i32 s2, s2, s62
	s_mov_b32 m0, s2
	ds_read_b128 v[180:183], v215 offset:16384
	ds_read_b128 v[184:187], v215 offset:17408
	ds_read_b128 v[204:207], v215 offset:18432
	ds_read_b128 v[216:219], v215 offset:19456
	ds_read_b128 v[220:223], v215 offset:20480
	ds_read_b128 v[224:227], v215 offset:21504
	ds_read_b128 v[228:231], v215 offset:22528
	ds_read_b128 v[232:235], v215 offset:23552
	global_load_lds_dwordx4 v156, s[18:19]
	s_add_i32 m0, s2, 0x2000
	s_add_u32 s2, s18, 0x40000
	s_addc_u32 s3, s19, 0
	s_add_i32 s8, s8, s62
	global_load_lds_dwordx4 v162, s[18:19]
	s_mov_b32 m0, s8
	global_load_lds_dwordx4 v156, s[2:3]
	s_add_i32 m0, s8, 0x2000
	s_nop 0
	global_load_lds_dwordx4 v162, s[2:3]
	s_mov_b32 m0, s22
	s_nop 0
	global_load_lds_dwordx4 v158, s[20:21]
	s_mov_b32 m0, s23
	s_nop 0
	global_load_lds_dwordx4 v164, s[20:21]
	s_waitcnt vmcnt(8)
	s_waitcnt lgkmcnt(0)
	s_barrier
	s_setprio 1
	s_waitcnt lgkmcnt(0)
	v_mfma_f32_16x16x32_bf16 v[60:63], v[128:131], v[180:183], v[60:63]
	v_mfma_f32_16x16x32_bf16 v[56:59], v[136:139], v[180:183], v[56:59]
	v_mfma_f32_16x16x32_bf16 v[44:47], v[128:131], v[204:207], v[44:47]
	v_mfma_f32_16x16x32_bf16 v[40:43], v[136:139], v[204:207], v[40:43]
	v_mfma_f32_16x16x32_bf16 v[28:31], v[128:131], v[220:223], v[28:31]
	v_mfma_f32_16x16x32_bf16 v[24:27], v[136:139], v[220:223], v[24:27]
	v_mfma_f32_16x16x32_bf16 v[12:15], v[128:131], v[228:231], v[12:15]
	v_mfma_f32_16x16x32_bf16 v[8:11], v[136:139], v[228:231], v[8:11]
	v_mfma_f32_16x16x32_bf16 v[60:63], v[132:135], v[184:187], v[60:63]
	v_mfma_f32_16x16x32_bf16 v[56:59], v[140:143], v[184:187], v[56:59]
	v_mfma_f32_16x16x32_bf16 v[44:47], v[132:135], v[216:219], v[44:47]
	v_mfma_f32_16x16x32_bf16 v[40:43], v[140:143], v[216:219], v[40:43]
	v_mfma_f32_16x16x32_bf16 v[28:31], v[132:135], v[224:227], v[28:31]
	v_mfma_f32_16x16x32_bf16 v[24:27], v[140:143], v[224:227], v[24:27]
	v_mfma_f32_16x16x32_bf16 v[12:15], v[132:135], v[232:235], v[12:15]
	v_mfma_f32_16x16x32_bf16 v[8:11], v[140:143], v[232:235], v[8:11]
	s_setprio 0
	s_setprio 1
	v_mfma_f32_16x16x32_bf16 v[52:55], v[144:147], v[180:183], v[52:55]
	v_mfma_f32_16x16x32_bf16 v[48:51], v[152:155], v[180:183], v[48:51]
	v_mfma_f32_16x16x32_bf16 v[36:39], v[144:147], v[204:207], v[36:39]
	v_mfma_f32_16x16x32_bf16 v[32:35], v[152:155], v[204:207], v[32:35]
	v_mfma_f32_16x16x32_bf16 v[20:23], v[144:147], v[220:223], v[20:23]
	v_mfma_f32_16x16x32_bf16 v[16:19], v[152:155], v[220:223], v[16:19]
	v_mfma_f32_16x16x32_bf16 v[4:7], v[144:147], v[228:231], v[4:7]
	v_mfma_f32_16x16x32_bf16 v[0:3], v[152:155], v[228:231], v[0:3]
	v_mfma_f32_16x16x32_bf16 v[52:55], v[148:151], v[184:187], v[52:55]
	v_mfma_f32_16x16x32_bf16 v[48:51], v[176:179], v[184:187], v[48:51]
	v_mfma_f32_16x16x32_bf16 v[36:39], v[148:151], v[216:219], v[36:39]
	v_mfma_f32_16x16x32_bf16 v[32:35], v[176:179], v[216:219], v[32:35]
	v_mfma_f32_16x16x32_bf16 v[20:23], v[148:151], v[224:227], v[20:23]
	v_mfma_f32_16x16x32_bf16 v[16:19], v[176:179], v[224:227], v[16:19]
	v_mfma_f32_16x16x32_bf16 v[4:7], v[148:151], v[232:235], v[4:7]
	v_mfma_f32_16x16x32_bf16 v[0:3], v[176:179], v[232:235], v[0:3]
	s_setprio 0
	s_barrier
; #define PG8_STAGE(bufoff, gbase, voff) do { _Pragma("unroll") for (int _i = 0; _i < 2; ++_i) \
;         __builtin_amdgcn_global_load_lds((const unsigned*)((const char*)(gbase) + (voff)[_i]), (LAS unsigned*)(lds + (bufoff) + ldsw + _i * 8192), 16, 0, 0); } while (0)
; #define PG8_STAGE_A(bufoff, gbase, h, nx) do { if constexpr (GATHER) { unsigned _v[2]; _v[0] = (nx) ? voffAn[h][0] : voffA[h][0]; _v[1] = (nx) ? voffAn[h][1] : voffA[h][1]; PG8_STAGE(bufoff, gbase, _v); } \
;         else PG8_STAGE(bufoff, (gbase) + (h) * hstepA, voffA[0]); } while (0)
; #define PG8_LDA(dst, b, h) do { _Pragma("unroll") for (int m = 0; m < 4; ++m) _Pragma("unroll") for (int k = 0; k < 2; ++k) dst[m][k] = *(const LAS bf16x8*)(lds + PG8_SA(b, h) + aoff + m * 2048 + k * 1024); } while (0)
; #define PG8_LDB(dst, b, h) do { _Pragma("unroll") for (int n = 0; n < 2; ++n) _Pragma("unroll") for (int k = 0; k < 2; ++k) dst[n][k] = *(const LAS bf16x8*)(lds + PG8_SB(b, h) + boff + n * 2048 + k * 1024); } while (0)
; #define PG8_MMA(ai, bj, At, Bt) do { __builtin_amdgcn_s_setprio(1); _Pragma("unroll") for (int m = 0; m < 4; ++m) _Pragma("unroll") for (int n = 0; n < 2; ++n) _Pragma("unroll") for (int k = 0; k < 2; ++k) \
;         acc[ai][bj][m][n] = __builtin_amdgcn_mfma_f32_16x16x32_bf16(Bt[n][k], At[m][k], acc[ai][bj][m][n], 0, 0, 0); __builtin_amdgcn_s_setprio(0); } while (0)
; #define PG8_WAIT_V(n) asm volatile("s_waitcnt vmcnt(" #n ")" ::: "memory")
; #define PG8_WAIT_L(n) asm volatile("s_waitcnt lgkmcnt(" #n ")" ::: "memory")
; #define PG8_BAR __builtin_amdgcn_s_barrier()
; #define PG8_SCHED __builtin_amdgcn_sched_barrier(0)
; template <class Epi, class Sched, bool GATHER, bool ALIGN_EPI>
; __device__ __forceinline__ void gemm_phase(LAS unsigned char* lds, const int wave_, const int K, const int lda, const int ldb, const Sched& S, const Epi& E) {
;     ...
;             PG8_LDB(B0, 1, 0); PG8_LDB(B1, 1, 1); PG8_SCHED; PG8_LDA(At, 1, 0); PG8_STAGE_A(PG8_SA(0, 1), a2, 1, last);
;             PG8_WAIT_V(8); PG8_WAIT_L(0); PG8_BAR; PG8_MMA(0, 0, At, B0); PG8_MMA(0, 1, At, B1); PG8_BAR; PG8_SCHED;
;             PG8_LDA(At, 1, 1); PG8_STAGE(PG8_SB(1, 0), b3, voffB); PG8_STAGE(PG8_SB(1, 1), b3 + hstepB, voffB); PG8_STAGE_A(PG8_SA(1, 0), a3, 0, last);
;             PG8_WAIT_V(8); PG8_WAIT_L(0); PG8_BAR; PG8_MMA(1, 0, At, B0); PG8_MMA(1, 1, At, B1); PG8_BAR; PG8_SCHED;
;         }
	s_add_i32 s8, 0, 0x18000
	s_add_i32 s9, 0, 0x1c000
	v_add_u32_e32 v140, s8, v201
	v_add_u32_e32 v160, s9, v201
	ds_read_b128 v[128:131], v140
	ds_read_b128 v[132:135], v140 offset:1024
	ds_read_b128 v[136:139], v140 offset:2048
	ds_read_b128 v[140:143], v140 offset:3072
	ds_read_b128 v[144:147], v160
	ds_read_b128 v[148:151], v160 offset:1024
	ds_read_b128 v[152:155], v160 offset:2048
	ds_read_b128 v[176:179], v160 offset:3072
	s_add_u32 s2, s20, 0x40000
	s_addc_u32 s3, s21, 0
	s_mov_b32 m0, s24
	ds_read_b128 v[180:183], v215 offset:32768
	ds_read_b128 v[184:187], v215 offset:33792
	ds_read_b128 v[204:207], v215 offset:34816
	ds_read_b128 v[216:219], v215 offset:35840
	ds_read_b128 v[220:223], v215 offset:36864
	ds_read_b128 v[224:227], v215 offset:37888
	ds_read_b128 v[228:231], v215 offset:38912
	ds_read_b128 v[232:235], v215 offset:39936
	global_load_lds_dwordx4 v158, s[2:3]
	s_mov_b32 m0, s25
	s_nop 0
	global_load_lds_dwordx4 v164, s[2:3]
	s_waitcnt vmcnt(8)
	s_waitcnt lgkmcnt(0)
	s_barrier
	s_setprio 1
	s_waitcnt lgkmcnt(0)
	v_mfma_f32_16x16x32_bf16 v[124:127], v[128:131], v[180:183], v[124:127]
	v_mfma_f32_16x16x32_bf16 v[120:123], v[136:139], v[180:183], v[120:123]
	v_mfma_f32_16x16x32_bf16 v[108:111], v[128:131], v[204:207], v[108:111]
	v_mfma_f32_16x16x32_bf16 v[104:107], v[136:139], v[204:207], v[104:107]
	v_mfma_f32_16x16x32_bf16 v[92:95], v[128:131], v[220:223], v[92:95]
	v_mfma_f32_16x16x32_bf16 v[88:91], v[136:139], v[220:223], v[88:91]
	v_mfma_f32_16x16x32_bf16 v[76:79], v[128:131], v[228:231], v[76:79]
	v_mfma_f32_16x16x32_bf16 v[72:75], v[136:139], v[228:231], v[72:75]
	v_mfma_f32_16x16x32_bf16 v[124:127], v[132:135], v[184:187], v[124:127]
	v_mfma_f32_16x16x32_bf16 v[120:123], v[140:143], v[184:187], v[120:123]
	v_mfma_f32_16x16x32_bf16 v[108:111], v[132:135], v[216:219], v[108:111]
	v_mfma_f32_16x16x32_bf16 v[104:107], v[140:143], v[216:219], v[104:107]
	v_mfma_f32_16x16x32_bf16 v[92:95], v[132:135], v[224:227], v[92:95]
	v_mfma_f32_16x16x32_bf16 v[88:91], v[140:143], v[224:227], v[88:91]
	v_mfma_f32_16x16x32_bf16 v[76:79], v[132:135], v[232:235], v[76:79]
	v_mfma_f32_16x16x32_bf16 v[72:75], v[140:143], v[232:235], v[72:75]
	s_setprio 0
	s_setprio 1
	v_mfma_f32_16x16x32_bf16 v[116:119], v[144:147], v[180:183], v[116:119]
	v_mfma_f32_16x16x32_bf16 v[112:115], v[152:155], v[180:183], v[112:115]
	v_mfma_f32_16x16x32_bf16 v[100:103], v[144:147], v[204:207], v[100:103]
	v_mfma_f32_16x16x32_bf16 v[96:99], v[152:155], v[204:207], v[96:99]
	v_mfma_f32_16x16x32_bf16 v[84:87], v[144:147], v[220:223], v[84:87]
	v_mfma_f32_16x16x32_bf16 v[80:83], v[152:155], v[220:223], v[80:83]
	v_mfma_f32_16x16x32_bf16 v[68:71], v[144:147], v[228:231], v[68:71]
	v_mfma_f32_16x16x32_bf16 v[64:67], v[152:155], v[228:231], v[64:67]
	v_mfma_f32_16x16x32_bf16 v[116:119], v[148:151], v[184:187], v[116:119]
	v_mfma_f32_16x16x32_bf16 v[112:115], v[176:179], v[184:187], v[112:115]
	v_mfma_f32_16x16x32_bf16 v[100:103], v[148:151], v[216:219], v[100:103]
	v_mfma_f32_16x16x32_bf16 v[96:99], v[176:179], v[216:219], v[96:99]
	v_mfma_f32_16x16x32_bf16 v[84:87], v[148:151], v[224:227], v[84:87]
	v_mfma_f32_16x16x32_bf16 v[80:83], v[176:179], v[224:227], v[80:83]
	v_mfma_f32_16x16x32_bf16 v[68:71], v[148:151], v[232:235], v[68:71]
	v_mfma_f32_16x16x32_bf16 v[64:67], v[176:179], v[232:235], v[64:67]
	s_setprio 0
	s_barrier
	s_add_i32 s2, s8, s62
	s_mov_b32 m0, s2
	ds_read_b128 v[180:183], v215 offset:49152
	ds_read_b128 v[184:187], v215 offset:50176
	ds_read_b128 v[204:207], v215 offset:51200
	ds_read_b128 v[216:219], v215 offset:52224
	ds_read_b128 v[220:223], v215 offset:53248
	ds_read_b128 v[224:227], v215 offset:54272
	ds_read_b128 v[228:231], v215 offset:55296
	ds_read_b128 v[232:235], v215 offset:56320
	s_add_u32 s98, s18, 0x80
	s_addc_u32 s99, s19, 0
	global_load_lds_dwordx4 v156, s[98:99]
	s_add_i32 m0, s2, 0x2000
	s_add_u32 s2, s18, 0x40080
	s_addc_u32 s3, s19, 0
	s_add_i32 s8, s9, s62
	global_load_lds_dwordx4 v162, s[98:99]
	s_mov_b32 m0, s8
	s_nop 0
	global_load_lds_dwordx4 v156, s[2:3]
	s_add_i32 m0, s8, 0x2000
	s_nop 0
	global_load_lds_dwordx4 v162, s[2:3]
	s_mov_b32 m0, s26
	s_nop 0
	s_add_u32 s96, s20, 0x80
	s_addc_u32 s97, s21, 0
	global_load_lds_dwordx4 v158, s[96:97]
	s_mov_b32 m0, s27
	s_nop 0
	global_load_lds_dwordx4 v164, s[96:97]
	s_waitcnt vmcnt(8)
	s_waitcnt lgkmcnt(0)
	s_barrier
	s_setprio 1
	s_waitcnt lgkmcnt(0)
	v_mfma_f32_16x16x32_bf16 v[60:63], v[128:131], v[180:183], v[60:63]
	v_mfma_f32_16x16x32_bf16 v[56:59], v[136:139], v[180:183], v[56:59]
	v_mfma_f32_16x16x32_bf16 v[44:47], v[128:131], v[204:207], v[44:47]
	v_mfma_f32_16x16x32_bf16 v[40:43], v[136:139], v[204:207], v[40:43]
	v_mfma_f32_16x16x32_bf16 v[28:31], v[128:131], v[220:223], v[28:31]
	v_mfma_f32_16x16x32_bf16 v[24:27], v[136:139], v[220:223], v[24:27]
	v_mfma_f32_16x16x32_bf16 v[12:15], v[128:131], v[228:231], v[12:15]
	v_mfma_f32_16x16x32_bf16 v[8:11], v[136:139], v[228:231], v[8:11]
	v_mfma_f32_16x16x32_bf16 v[60:63], v[132:135], v[184:187], v[60:63]
	v_mfma_f32_16x16x32_bf16 v[56:59], v[140:143], v[184:187], v[56:59]
	v_mfma_f32_16x16x32_bf16 v[44:47], v[132:135], v[216:219], v[44:47]
	v_mfma_f32_16x16x32_bf16 v[40:43], v[140:143], v[216:219], v[40:43]
	v_mfma_f32_16x16x32_bf16 v[28:31], v[132:135], v[224:227], v[28:31]
	v_mfma_f32_16x16x32_bf16 v[24:27], v[140:143], v[224:227], v[24:27]
	v_mfma_f32_16x16x32_bf16 v[12:15], v[132:135], v[232:235], v[12:15]
	v_mfma_f32_16x16x32_bf16 v[8:11], v[140:143], v[232:235], v[8:11]
	s_setprio 0
	s_setprio 1
	v_mfma_f32_16x16x32_bf16 v[52:55], v[144:147], v[180:183], v[52:55]
	v_mfma_f32_16x16x32_bf16 v[48:51], v[152:155], v[180:183], v[48:51]
	v_mfma_f32_16x16x32_bf16 v[36:39], v[144:147], v[204:207], v[36:39]
	v_mfma_f32_16x16x32_bf16 v[32:35], v[152:155], v[204:207], v[32:35]
	v_mfma_f32_16x16x32_bf16 v[20:23], v[144:147], v[220:223], v[20:23]
	v_mfma_f32_16x16x32_bf16 v[16:19], v[152:155], v[220:223], v[16:19]
	v_mfma_f32_16x16x32_bf16 v[4:7], v[144:147], v[228:231], v[4:7]
	v_mfma_f32_16x16x32_bf16 v[0:3], v[152:155], v[228:231], v[0:3]
	v_mfma_f32_16x16x32_bf16 v[52:55], v[148:151], v[184:187], v[52:55]
	v_mfma_f32_16x16x32_bf16 v[48:51], v[176:179], v[184:187], v[48:51]
	v_mfma_f32_16x16x32_bf16 v[36:39], v[148:151], v[216:219], v[36:39]
	v_mfma_f32_16x16x32_bf16 v[32:35], v[176:179], v[216:219], v[32:35]
	v_mfma_f32_16x16x32_bf16 v[20:23], v[148:151], v[224:227], v[20:23]
	v_mfma_f32_16x16x32_bf16 v[16:19], v[176:179], v[224:227], v[16:19]
	v_mfma_f32_16x16x32_bf16 v[4:7], v[148:151], v[232:235], v[4:7]
	v_mfma_f32_16x16x32_bf16 v[0:3], v[176:179], v[232:235], v[0:3]
	s_setprio 0
	s_barrier
	s_add_i32 s31, s31, 2
	s_add_u32 s4, s4, 0x100
	s_addc_u32 s5, s5, 0
	s_add_u32 s11, s11, 0x100
	s_addc_u32 s13, s13, 0
	s_cmp_gt_u32 s31, 13
	s_cbranch_scc0 .LBB0_720
	v_readlane_b32 s2, v253, 1
	v_readlane_b32 s3, v253, 2
	s_and_b64 vcc, exec, s[2:3]
	s_cbranch_vccz .LBB0_723
	s_barrier
